# baseline (speedup 1.0000x reference)
_Z7k_fine3PKfS0_PKtS2_PKdS4_S0_PiPfS5_S0_S0_PtS7_:
	s_load_dwordx2 s[4:5], s[0:1], 0x30
	s_load_dwordx8 s[68:75], s[0:1], 0x0
	s_load_dwordx2 s[88:89], s[0:1], 0x48
	s_load_dwordx4 s[80:83], s[0:1], 0x20
	s_load_dwordx8 s[60:67], s[0:1], 0x50
	s_lshl_b32 s3, s2, 5
	s_and_b32 s3, s3, 0xe0
	s_lshr_b32 s76, s2, 3
	s_add_i32 s3, s3, s76
	s_lshr_b32 s84, s3, 1
	s_mov_b32 s85, 0
	s_lshl_b64 s[6:7], s[84:85], 14
	s_waitcnt lgkmcnt(0)
	s_and_b32 s90, s84, 56
	s_lshl_b32 s91, s84, 3
	s_and_b32 s91, s91, 56
	s_or_b32 s90, s90, 4
	s_or_b32 s91, s91, 4
	s_lshr_b32 s92, s3, 7
	s_lshl_b32 s92, s92, 12
	s_lshl_b32 s93, s90, 6
	s_add_i32 s93, s93, s91
	s_add_i32 s93, s93, s92
	s_lshl_b32 s93, s93, 3
	s_add_u32 s96, s80, s93
	s_addc_u32 s97, s81, 0
	s_load_dwordx2 s[96:97], s[96:97], 0x0
	v_subrev_u32_e32 v165, 63, v0
	v_max_i32_e32 v165, 1, v165
	v_min_i32_e32 v165, 3, v165
	v_mul_u32_u24_e32 v166, 0x208, v165
	v_mul_u32_u24_e32 v167, 0x1f8, v165
	v_lshlrev_b32_e32 v168, 9, v165
	v_lshlrev_b32_e32 v169, 3, v165
	v_sub_u32_e32 v170, s93, v166
	global_load_dwordx2 v[172:173], v170, s[80:81]
	v_sub_u32_e32 v170, s93, v168
	global_load_dwordx2 v[174:175], v170, s[80:81]
	v_sub_u32_e32 v170, s93, v167
	global_load_dwordx2 v[176:177], v170, s[80:81]
	v_sub_u32_e32 v170, s93, v169
	global_load_dwordx2 v[178:179], v170, s[80:81]
	v_add_u32_e32 v170, s93, v169
	global_load_dwordx2 v[180:181], v170, s[80:81]
	v_add_u32_e32 v170, s93, v167
	global_load_dwordx2 v[182:183], v170, s[80:81]
	v_add_u32_e32 v170, s93, v168
	global_load_dwordx2 v[184:185], v170, s[80:81]
	v_add_u32_e32 v170, s93, v166
	global_load_dwordx2 v[186:187], v170, s[80:81]
	s_add_u32 s4, s4, s6
	s_addc_u32 s5, s5, s7
	v_lshlrev_b32_e32 v2, 2, v0
	v_mov_b32_e32 v3, 0
	v_lshl_add_u64 v[4:5], s[4:5], 0, v[2:3]
	s_mov_b32 s6, 0x200000
	v_add_co_u32_e32 v6, vcc, s6, v4
	s_mov_b32 s7, 0x400000
	s_nop 0
	v_addc_co_u32_e32 v7, vcc, 0, v5, vcc
	v_or_b32_e32 v117, 0x400, v0
	v_add_co_u32_e32 v8, vcc, s7, v4
	v_lshlrev_b32_e32 v10, 2, v117
	v_mov_b32_e32 v11, v3
	v_addc_co_u32_e32 v9, vcc, 0, v5, vcc
	v_lshl_add_u64 v[12:13], s[4:5], 0, v[10:11]
	v_add_co_u32_e32 v14, vcc, s6, v12
	s_movk_i32 s8, 0x1000
	s_nop 0
	v_addc_co_u32_e32 v15, vcc, 0, v13, vcc
	v_add_co_u32_e32 v12, vcc, s7, v12
	v_or_b32_e32 v118, 0x800, v0
	s_nop 0
	v_addc_co_u32_e32 v13, vcc, 0, v13, vcc
	v_add_co_u32_e32 v16, vcc, s8, v4
	s_mov_b32 s8, 0x201000
	s_nop 0
	v_addc_co_u32_e32 v17, vcc, 0, v5, vcc
	v_add_co_u32_e32 v18, vcc, s8, v4
	s_mov_b32 s8, 0x401000
	s_nop 0
	v_addc_co_u32_e32 v19, vcc, 0, v5, vcc
	global_load_dword v24, v[6:7], off nt
	global_load_dword v25, v[8:9], off nt
	global_load_dword v26, v[8:9], off offset:2048 nt
	global_load_dword v27, v[14:15], off nt
	global_load_dword v28, v[12:13], off nt
	global_load_dword v29, v[16:17], off offset:2048 nt
	global_load_dword v30, v[18:19], off offset:2048 nt
	global_load_dword v31, v[6:7], off offset:2048 nt
	v_add_co_u32_e32 v6, vcc, s8, v4
	v_lshlrev_b32_e32 v8, 2, v118
	v_mov_b32_e32 v9, v3
	v_addc_co_u32_e32 v7, vcc, 0, v5, vcc
	v_lshl_add_u64 v[12:13], s[4:5], 0, v[8:9]
	global_load_dword v32, v2, s[4:5] nt
	global_load_dword v33, v2, s[4:5] offset:2048 nt
	global_load_dword v34, v10, s[4:5] nt
	global_load_dword v35, v8, s[4:5] nt
	v_add_co_u32_e32 v8, vcc, s6, v12
	s_movk_i32 s8, 0x2000
	s_nop 0
	v_addc_co_u32_e32 v9, vcc, 0, v13, vcc
	v_add_co_u32_e32 v10, vcc, s7, v12
	v_or_b32_e32 v1, 0xc00, v0
	s_nop 0
	v_addc_co_u32_e32 v11, vcc, 0, v13, vcc
	v_add_co_u32_e32 v12, vcc, s8, v4
	s_mov_b32 s8, 0x202000
	s_nop 0
	v_addc_co_u32_e32 v13, vcc, 0, v5, vcc
	v_add_co_u32_e32 v14, vcc, s8, v4
	s_mov_b32 s8, 0x402000
	s_nop 0
	v_addc_co_u32_e32 v15, vcc, 0, v5, vcc
	v_add_co_u32_e32 v16, vcc, s8, v4
	v_lshlrev_b32_e32 v18, 2, v1
	v_mov_b32_e32 v19, v3
	v_addc_co_u32_e32 v17, vcc, 0, v5, vcc
	v_lshl_add_u64 v[20:21], s[4:5], 0, v[18:19]
	v_add_co_u32_e32 v22, vcc, s6, v20
	s_movk_i32 s6, 0x3000
	s_nop 0
	v_addc_co_u32_e32 v23, vcc, 0, v21, vcc
	v_add_co_u32_e32 v20, vcc, s7, v20
	v_and_b32_e32 v124, 63, v0
	s_nop 0
	v_addc_co_u32_e32 v21, vcc, 0, v21, vcc
	global_load_dword v3, v[6:7], off offset:2048 nt
	global_load_dword v19, v[8:9], off nt
	global_load_dword v36, v[10:11], off nt
	global_load_dword v37, v[12:13], off offset:2048 nt
	global_load_dword v38, v[14:15], off offset:2048 nt
	global_load_dword v39, v[16:17], off offset:2048 nt
	global_load_dword v40, v[22:23], off nt
	global_load_dword v41, v[20:21], off nt
	v_add_co_u32_e32 v6, vcc, s6, v4
	s_mov_b32 s6, 0x203000
	s_nop 0
	v_addc_co_u32_e32 v7, vcc, 0, v5, vcc
	v_add_co_u32_e32 v8, vcc, s6, v4
	s_mov_b32 s6, 0x403000
	s_nop 0
	v_addc_co_u32_e32 v9, vcc, 0, v5, vcc
	v_add_co_u32_e32 v4, vcc, s6, v4
	v_lshrrev_b32_e32 v116, 6, v0
	s_nop 0
	v_addc_co_u32_e32 v5, vcc, 0, v5, vcc
	global_load_dword v13, v18, s[4:5] nt
	global_load_dword v14, v[6:7], off offset:2048 nt
	global_load_dword v15, v[8:9], off offset:2048 nt
	global_load_dword v16, v[4:5], off offset:2048 nt
	s_and_b32 s90, s84, 56
	s_lshl_b32 s91, s84, 3
	s_and_b32 s91, s91, 56
	s_or_b32 s90, s90, 4
	s_or_b32 s91, s91, 4
	s_lshr_b32 s92, s3, 7
	s_lshl_b32 s92, s92, 12
	v_lshrrev_b32_e32 v216, 5, v0
	v_mul_u32_u24_e32 v217, 57, v216
	v_lshrrev_b32_e32 v217, 9, v217
	v_mad_i32_i24 v216, v217, -9, v216
	v_add_u32_e32 v218, 1, v217
	v_mul_u32_u24_e32 v217, 0xab, v216
	v_lshrrev_b32_e32 v217, 9, v217
	v_mad_i32_i24 v216, v217, -3, v216
	v_add_u32_e32 v217, -1, v217
	v_add_u32_e32 v216, -1, v216
	v_mad_i32_i24 v217, v217, v218, s90
	v_mad_i32_i24 v216, v216, v218, s91
	v_lshl_add_u32 v217, v217, 6, v216
	v_add_u32_e32 v217, s92, v217
	v_and_b32_e32 v216, 31, v0
	v_lshlrev_b32_e32 v217, 9, v217
	v_lshl_add_u32 v217, v216, 4, v217
	global_load_dwordx4 v[220:223], v217, s[68:69]
	v_add_u32_e32 v219, 0x200, v0
	v_min_u32_e32 v219, 0x35f, v219
	v_lshrrev_b32_e32 v216, 5, v219
	v_mul_u32_u24_e32 v217, 57, v216
	v_lshrrev_b32_e32 v217, 9, v217
	v_mad_i32_i24 v216, v217, -9, v216
	v_add_u32_e32 v218, 1, v217
	v_mul_u32_u24_e32 v217, 0xab, v216
	v_lshrrev_b32_e32 v217, 9, v217
	v_mad_i32_i24 v216, v217, -3, v216
	v_add_u32_e32 v217, -1, v217
	v_add_u32_e32 v216, -1, v216
	v_mad_i32_i24 v217, v217, v218, s90
	v_mad_i32_i24 v216, v216, v218, s91
	v_lshl_add_u32 v217, v217, 6, v216
	v_add_u32_e32 v217, s92, v217
	v_and_b32_e32 v216, 31, v219
	v_lshlrev_b32_e32 v217, 9, v217
	v_lshl_add_u32 v217, v216, 4, v217
	global_load_dwordx4 v[224:227], v217, s[68:69]
	s_and_b32 s94, s76, 1
	s_lshl_b32 s94, s94, 2
	s_add_i32 s94, s94, s90
	s_add_i32 s94, s94, -5
	s_add_i32 s95, s91, -5
	v_mov_b32_e32 v250, v0
	v_lshrrev_b32_e32 v251, 5, v250
	v_and_b32_e32 v252, 31, v250
	v_mul_u32_u24_e32 v253, 0xcd, v251
	v_lshrrev_b32_e32 v253, 11, v253
	v_mad_i32_i24 v254, v253, -10, v251
	v_add_u32_e32 v253, s94, v253
	v_add_u32_e32 v254, s95, v254
	v_med3_i32 v253, v253, 0, 63
	v_med3_i32 v254, v254, 0, 63
	v_lshl_add_u32 v253, v253, 6, v254
	v_add_u32_e32 v253, s92, v253
	v_lshlrev_b32_e32 v253, 9, v253
	v_lshl_add_u32 v253, v252, 4, v253
	global_load_dwordx4 v[234:237], v253, s[68:69]
	v_add_u32_e32 v250, 0x200, v0
	v_lshrrev_b32_e32 v251, 5, v250
	v_and_b32_e32 v252, 31, v250
	v_mul_u32_u24_e32 v253, 0xcd, v251
	v_lshrrev_b32_e32 v253, 11, v253
	v_mad_i32_i24 v254, v253, -10, v251
	v_add_u32_e32 v253, s94, v253
	v_add_u32_e32 v254, s95, v254
	v_med3_i32 v253, v253, 0, 63
	v_med3_i32 v254, v254, 0, 63
	v_lshl_add_u32 v253, v253, 6, v254
	v_add_u32_e32 v253, s92, v253
	v_lshlrev_b32_e32 v253, 9, v253
	v_lshl_add_u32 v253, v252, 4, v253
	global_load_dwordx4 v[238:241], v253, s[68:69]
	v_add_u32_e32 v250, 0x400, v0
	v_lshrrev_b32_e32 v251, 5, v250
	v_and_b32_e32 v252, 31, v250
	v_mul_u32_u24_e32 v253, 0xcd, v251
	v_lshrrev_b32_e32 v253, 11, v253
	v_mad_i32_i24 v254, v253, -10, v251
	v_add_u32_e32 v253, s94, v253
	v_add_u32_e32 v254, s95, v254
	v_med3_i32 v253, v253, 0, 63
	v_med3_i32 v254, v254, 0, 63
	v_lshl_add_u32 v253, v253, 6, v254
	v_add_u32_e32 v253, s92, v253
	v_lshlrev_b32_e32 v253, 9, v253
	v_lshl_add_u32 v253, v252, 4, v253
	global_load_dwordx4 v[242:245], v253, s[68:69]
	v_add_u32_e32 v250, 0x600, v0
	v_min_u32_e32 v250, 0x77f, v250
	v_lshrrev_b32_e32 v251, 5, v250
	v_and_b32_e32 v252, 31, v250
	v_mul_u32_u24_e32 v253, 0xcd, v251
	v_lshrrev_b32_e32 v253, 11, v253
	v_mad_i32_i24 v254, v253, -10, v251
	v_add_u32_e32 v253, s94, v253
	v_add_u32_e32 v254, s95, v254
	v_med3_i32 v253, v253, 0, 63
	v_med3_i32 v254, v254, 0, 63
	v_lshl_add_u32 v253, v253, 6, v254
	v_add_u32_e32 v253, s92, v253
	v_lshlrev_b32_e32 v253, 9, v253
	v_lshl_add_u32 v253, v252, 4, v253
	global_load_dwordx4 v[246:249], v253, s[68:69]
	v_subrev_u32_e32 v188, 64, v0
	v_cmp_gt_u32_e32 vcc, 3, v188
	s_and_saveexec_b64 s[98:99], vcc
	s_cbranch_execz .Lmy_invl0_done
	s_mov_b32 s6, 0
	s_brev_b32 s7, 8
	s_mov_b32 s8, 0x812dea11
	s_mov_b32 s9, 0x3d719799
	v_mov_b32_e32 v189, 0x100
	v_mov_b32_e32 v207, 0xffffff80
	v_mov_b32_e32 v208, 0x260
	v_lshlrev_b32_e32 v209, 3, v0
	s_waitcnt vmcnt(30) lgkmcnt(0)
	v_add_f64 v[192:193], v[172:173], 0
	v_add_f64 v[192:193], v[192:193], v[174:175]
	v_add_f64 v[192:193], v[192:193], v[176:177]
	v_add_f64 v[192:193], v[192:193], v[178:179]
	v_add_f64 v[192:193], v[192:193], s[96:97]
	v_add_f64 v[192:193], v[192:193], v[180:181]
	v_add_f64 v[192:193], v[192:193], v[182:183]
	v_add_f64 v[192:193], v[192:193], v[184:185]
	v_add_f64 v[190:191], v[192:193], v[186:187]
	v_cmp_gt_f64_e32 vcc, s[6:7], v[190:191]
	s_nop 1
	v_cndmask_b32_e32 v189, 0, v189, vcc
	v_ldexp_f64 v[190:191], v[190:191], v189
	v_rsq_f64_e32 v[192:193], v[190:191]
	v_cndmask_b32_e32 v189, 0, v207, vcc
	v_cmp_class_f64_e32 vcc, v[190:191], v208
	v_mul_f64 v[194:195], v[190:191], v[192:193]
	v_mul_f64 v[192:193], v[192:193], 0.5
	v_fma_f64 v[196:197], -v[192:193], v[194:195], 0.5
	v_fmac_f64_e32 v[194:195], v[194:195], v[196:197]
	v_fmac_f64_e32 v[192:193], v[192:193], v[196:197]
	v_fma_f64 v[196:197], -v[194:195], v[194:195], v[190:191]
	v_fmac_f64_e32 v[194:195], v[196:197], v[192:193]
	v_fma_f64 v[196:197], -v[194:195], v[194:195], v[190:191]
	v_fmac_f64_e32 v[194:195], v[196:197], v[192:193]
	v_ldexp_f64 v[192:193], v[194:195], v189
	v_cndmask_b32_e32 v191, v193, v191, vcc
	v_cndmask_b32_e32 v190, v192, v190, vcc
	v_max_f64 v[190:191], v[190:191], s[8:9]
	v_div_scale_f64 v[192:193], s[12:13], v[190:191], v[190:191], 1.0
	v_rcp_f64_e32 v[194:195], v[192:193]
	v_div_scale_f64 v[196:197], vcc, 1.0, v[190:191], 1.0
	v_fma_f64 v[198:199], -v[192:193], v[194:195], 1.0
	v_fmac_f64_e32 v[194:195], v[194:195], v[198:199]
	v_fma_f64 v[198:199], -v[192:193], v[194:195], 1.0
	v_fmac_f64_e32 v[194:195], v[194:195], v[198:199]
	v_mul_f64 v[198:199], v[196:197], v[194:195]
	v_fma_f64 v[192:193], -v[192:193], v[198:199], v[196:197]
	v_div_fmas_f64 v[192:193], v[192:193], v[194:195], v[198:199]
	v_div_fixup_f64 v[190:191], v[192:193], v[190:191], 1.0
	ds_write_b64 v209, v[190:191] offset:64512
.Lmy_invl0_done:
	s_or_b64 exec, exec, s[98:99]
	s_mov_b32 s4, 0xff800000
	v_cmp_eq_u32_e64 s[42:43], 0, v124
	s_waitcnt vmcnt(21)
	v_add_f32_e32 v4, v32, v24
	v_add_f32_e32 v12, v4, v25
	s_waitcnt vmcnt(20)
	v_add_f32_e32 v4, v33, v31
	s_waitcnt vmcnt(19)
	v_add_f32_e32 v5, v34, v27
	v_add_f32_e32 v11, v4, v26
	v_add_f32_e32 v10, v5, v28
	v_add_f32_e32 v5, v29, v30
	v_max3_f32 v4, v12, s4, v11
	s_waitcnt vmcnt(17)
	v_add_f32_e32 v9, v5, v3
	v_max3_f32 v3, v4, v10, v9
	s_waitcnt vmcnt(16)
	v_add_f32_e32 v4, v35, v19
	s_waitcnt vmcnt(15)
	v_add_f32_e32 v8, v4, v36
	s_waitcnt vmcnt(13)
	v_add_f32_e32 v4, v37, v38
	v_mbcnt_lo_u32_b32 v5, -1, 0
	s_waitcnt vmcnt(12)
	v_add_f32_e32 v7, v4, v39
	v_mbcnt_hi_u32_b32 v5, -1, v5
	v_max3_f32 v4, v3, v8, v7
	s_waitcnt vmcnt(9)
	v_add_f32_e32 v3, v13, v40
	v_and_b32_e32 v13, 64, v5
	v_add_f32_e32 v6, v3, v41
	s_waitcnt vmcnt(7)
	v_add_f32_e32 v3, v14, v15
	v_add_u32_e32 v13, 64, v13
	v_xor_b32_e32 v14, 1, v5
	v_cmp_lt_i32_e32 vcc, v14, v13
	s_waitcnt vmcnt(6)
	v_add_f32_e32 v3, v3, v16
	v_max3_f32 v4, v4, v6, v3
	v_cndmask_b32_e32 v14, v5, v14, vcc
	v_lshlrev_b32_e32 v115, 2, v14
	s_nop 1
	v_mov_b32_dpp v14, v4 quad_perm:[1,0,3,2] row_mask:0xf bank_mask:0xf
	s_waitcnt lgkmcnt(0)
	v_max_f32_e32 v14, v14, v14
	v_max_f32_e32 v4, v4, v14
	v_xor_b32_e32 v14, 2, v5
	v_cmp_lt_i32_e32 vcc, v14, v13
	s_nop 1
	v_cndmask_b32_e32 v14, v5, v14, vcc
	v_lshlrev_b32_e32 v114, 2, v14
	s_nop 1
	v_mov_b32_dpp v14, v4 quad_perm:[2,3,0,1] row_mask:0xf bank_mask:0xf
	s_waitcnt lgkmcnt(0)
	v_max_f32_e32 v14, v14, v14
	v_max_f32_e32 v4, v4, v14
	v_xor_b32_e32 v14, 4, v5
	v_cmp_lt_i32_e32 vcc, v14, v13
	s_nop 1
	v_cndmask_b32_e32 v14, v5, v14, vcc
	v_lshlrev_b32_e32 v113, 2, v14
	s_nop 1
	v_mov_b32_dpp v14, v4 row_half_mirror row_mask:0xf bank_mask:0xf
	s_waitcnt lgkmcnt(0)
	v_max_f32_e32 v14, v14, v14
	v_max_f32_e32 v4, v4, v14
	v_xor_b32_e32 v14, 8, v5
	v_cmp_lt_i32_e32 vcc, v14, v13
	s_nop 1
	v_cndmask_b32_e32 v14, v5, v14, vcc
	v_lshlrev_b32_e32 v112, 2, v14
	s_nop 1
	v_mov_b32_dpp v14, v4 row_mirror row_mask:0xf bank_mask:0xf
	s_waitcnt lgkmcnt(0)
	v_max_f32_e32 v14, v14, v14
	v_max_f32_e32 v4, v4, v14
	v_xor_b32_e32 v14, 16, v5
	v_cmp_lt_i32_e32 vcc, v14, v13
	s_nop 1
	v_cndmask_b32_e32 v14, v5, v14, vcc
	v_lshlrev_b32_e32 v122, 2, v14
	ds_bpermute_b32 v14, v122, v4
	s_waitcnt lgkmcnt(0)
	v_max_f32_e32 v14, v14, v14
	v_max_f32_e32 v4, v4, v14
	v_xor_b32_e32 v14, 32, v5
	v_cmp_lt_i32_e32 vcc, v14, v13
	s_nop 1
	v_cndmask_b32_e32 v5, v5, v14, vcc
	v_lshlrev_b32_e32 v121, 2, v5
	ds_bpermute_b32 v5, v121, v4
	s_and_saveexec_b64 s[4:5], s[42:43]
	s_cbranch_execz .LBB2_2
	s_waitcnt lgkmcnt(0)
	v_max_f32_e32 v5, v5, v5
	v_max_f32_e32 v4, v4, v4
	v_lshl_add_u32 v13, v116, 2, 0
	v_max_f32_e32 v4, v4, v5
	ds_write_b32 v13, v4 offset:65056
.LBB2_2:
	s_or_b64 exec, exec, s[4:5]
	v_cmp_eq_u32_e32 vcc, 0, v0
	s_and_saveexec_b64 s[4:5], vcc
	v_mov_b32_e32 v4, 0
	ds_write_b32 v4, v4 offset:65088
	s_or_b64 exec, exec, s[4:5]
	s_lshl_b32 s4, s84, 3
	s_and_b32 s77, s84, 56
	s_and_b32 s33, s4, 56
	s_movk_i32 s4, 0x360
	s_lshr_b32 s86, s3, 7
	s_or_b32 s10, s77, 4
	s_or_b32 s11, s33, 4
	s_mov_b32 s87, 0
	s_lshl_b64 s[6:7], s[86:87], 12
	s_mov_b64 s[8:9], 0
	s_movk_i32 s12, 0xab
	s_movk_i32 s13, 0x15f
	v_lshlrev_b32_e32 v228, 4, v0
	s_waitcnt vmcnt(5) lgkmcnt(0)
	ds_write_b128 v228, v[220:223]
	s_movk_i32 s4, 0x160
	v_cmp_gt_u32_e32 vcc, s4, v0
	s_and_saveexec_b64 s[4:5], vcc
	s_waitcnt vmcnt(4)
	ds_write_b128 v228, v[224:227] offset:8192
	s_or_b64 exec, exec, s[4:5]
	s_waitcnt vmcnt(0)
	v_mov_b32_e32 v250, v0
	v_lshrrev_b32_e32 v251, 5, v250
	v_and_b32_e32 v252, 31, v250
	v_lshlrev_b32_e32 v251, 9, v251
	v_and_b32_e32 v253, 1, v252
	v_lshrrev_b32_e32 v252, 1, v252
	v_lshl_add_u32 v251, v253, 8, v251
	v_lshl_add_u32 v251, v252, 4, v251
	v_add_u32_e32 v251, 0x13e00, v251
	ds_write_b128 v251, v[234:237]
	v_add_u32_e32 v250, 0x200, v0
	v_lshrrev_b32_e32 v251, 5, v250
	v_and_b32_e32 v252, 31, v250
	v_lshlrev_b32_e32 v251, 9, v251
	v_and_b32_e32 v253, 1, v252
	v_lshrrev_b32_e32 v252, 1, v252
	v_lshl_add_u32 v251, v253, 8, v251
	v_lshl_add_u32 v251, v252, 4, v251
	v_add_u32_e32 v251, 0x13e00, v251
	ds_write_b128 v251, v[238:241]
	v_add_u32_e32 v250, 0x400, v0
	v_lshrrev_b32_e32 v251, 5, v250
	v_and_b32_e32 v252, 31, v250
	v_lshlrev_b32_e32 v251, 9, v251
	v_and_b32_e32 v253, 1, v252
	v_lshrrev_b32_e32 v252, 1, v252
	v_lshl_add_u32 v251, v253, 8, v251
	v_lshl_add_u32 v251, v252, 4, v251
	v_add_u32_e32 v251, 0x13e00, v251
	ds_write_b128 v251, v[242:245]
	v_add_u32_e32 v250, 0x600, v0
	v_lshrrev_b32_e32 v251, 5, v250
	v_and_b32_e32 v252, 31, v250
	v_lshlrev_b32_e32 v251, 9, v251
	v_and_b32_e32 v253, 1, v252
	v_lshrrev_b32_e32 v252, 1, v252
	v_lshl_add_u32 v251, v253, 8, v251
	v_lshl_add_u32 v251, v252, 4, v251
	v_add_u32_e32 v251, 0x13e00, v251
	v_cmp_gt_u32_e32 vcc, 0x180, v0
	s_and_saveexec_b64 s[98:99], vcc
	ds_write_b128 v251, v[246:249]
	s_or_b64 exec, exec, s[98:99]
	s_load_dwordx4 s[4:7], s[0:1], 0x38
	v_subrev_u32_e32 v2, 64, v0
	v_cmp_gt_u32_e32 vcc, 3, v2
	v_lshl_add_u32 v119, v0, 3, 0
	s_waitcnt lgkmcnt(0)
	v_writelane_b32 v212, s4, 0
	s_nop 1
	v_writelane_b32 v212, s5, 1
	v_writelane_b32 v212, s6, 2
	v_writelane_b32 v212, s7, 3
	s_and_saveexec_b64 s[0:1], vcc
	s_cbranch_execz .LBB2_9
.LBB2_9:
	s_or_b64 exec, exec, s[0:1]
	v_mov_b32_e32 v2, 0
	s_waitcnt lgkmcnt(0)
	s_barrier
	ds_read_b128 v[14:17], v2 offset:65056
	ds_read_b128 v[18:21], v2 offset:65072
	s_waitcnt lgkmcnt(1)
	v_max_f32_e32 v2, v15, v15
	v_max_f32_e32 v4, v14, v14
	v_max_f32_e32 v2, v4, v2
	v_max3_f32 v2, v2, v16, v17
	s_waitcnt lgkmcnt(0)
	v_max3_f32 v2, v2, v18, v19
	v_max3_f32 v2, v2, v20, v21
	v_add_f32_e32 v2, 0xbbd844d0, v2
	v_cmp_ge_f32_e32 vcc, v12, v2
	s_and_saveexec_b64 s[0:1], vcc
	s_cbranch_execz .LBB2_13
	s_mov_b64 s[6:7], exec
	v_mbcnt_lo_u32_b32 v4, s6, 0
	v_mbcnt_hi_u32_b32 v4, s7, v4
	v_cmp_eq_u32_e32 vcc, 0, v4
	s_and_saveexec_b64 s[4:5], vcc
	s_bcnt1_i32_b64 s6, s[6:7]
	v_mov_b32_e32 v5, 0
	v_mov_b32_e32 v12, s6
	ds_add_rtn_u32 v5, v5, v12 offset:65088
	s_or_b64 exec, exec, s[4:5]
	s_waitcnt lgkmcnt(0)
	v_readfirstlane_b32 s4, v5
	s_nop 1
	v_add_u32_e32 v4, s4, v4
	v_lshl_add_u32 v4, v4, 2, 0
	ds_write_b32 v4, v0 offset:13824
